# v31 plus fast tile step extended to causally masked tiles and the first tile of each pass
# baseline (speedup 1.0000x reference)
.LBB0_556:
	s_setprio 3
	ds_read_b128 v[116:119], v189 offset:0
	ds_read_b128 v[120:123], v226 offset:0
	ds_read_b128 v[124:127], v227 offset:0
	ds_read_b128 v[128:131], v228 offset:0
	s_waitcnt lgkmcnt(3)
	v_mfma_f32_32x32x16_bf16 v[84:99], v[116:119], v[132:135], 0
	ds_read_b128 v[116:119], v232 offset:0
	s_waitcnt lgkmcnt(3)
	v_mfma_f32_32x32x16_bf16 v[84:99], v[120:123], v[136:139], v[84:99]
	ds_read_b128 v[120:123], v233 offset:0
	s_waitcnt lgkmcnt(3)
	v_mfma_f32_32x32x16_bf16 v[84:99], v[124:127], v[140:143], v[84:99]
	ds_read_b128 v[124:127], v234 offset:0
	s_waitcnt lgkmcnt(3)
	v_mfma_f32_32x32x16_bf16 v[84:99], v[128:131], v[144:147], v[84:99]
	ds_read_b128 v[128:131], v235 offset:0
	s_waitcnt lgkmcnt(3)
	v_mfma_f32_32x32x16_bf16 v[84:99], v[116:119], v[148:151], v[84:99]
	ds_read_b128 v[116:119], v190 offset:0
	s_waitcnt lgkmcnt(3)
	v_mfma_f32_32x32x16_bf16 v[84:99], v[120:123], v[152:155], v[84:99]
	ds_read_b128 v[120:123], v229 offset:0
	s_waitcnt lgkmcnt(3)
	v_mfma_f32_32x32x16_bf16 v[84:99], v[124:127], v[156:159], v[84:99]
	ds_read_b128 v[124:127], v230 offset:0
	s_waitcnt lgkmcnt(3)
	v_mfma_f32_32x32x16_bf16 v[84:99], v[128:131], v[160:163], v[84:99]
	ds_read_b128 v[128:131], v231 offset:0
	s_waitcnt lgkmcnt(3)
	v_mfma_f32_32x32x16_bf16 v[84:99], v[116:119], v[164:167], v[84:99]
	ds_read_b128 v[116:119], v189 offset:8192
	s_waitcnt lgkmcnt(3)
	v_mfma_f32_32x32x16_bf16 v[84:99], v[120:123], v[172:175], v[84:99]
	ds_read_b128 v[120:123], v226 offset:8192
	s_waitcnt lgkmcnt(3)
	v_mfma_f32_32x32x16_bf16 v[84:99], v[124:127], v[168:171], v[84:99]
	ds_read_b128 v[124:127], v227 offset:8192
	s_waitcnt lgkmcnt(3)
	v_mfma_f32_32x32x16_bf16 v[84:99], v[128:131], v[176:179], v[84:99]
	ds_read_b128 v[128:131], v228 offset:8192
	s_waitcnt lgkmcnt(3)
	v_mfma_f32_32x32x16_bf16 v[68:83], v[116:119], v[132:135], 0
	ds_read_b128 v[116:119], v232 offset:8192
	s_waitcnt lgkmcnt(3)
	v_mfma_f32_32x32x16_bf16 v[68:83], v[120:123], v[136:139], v[68:83]
	ds_read_b128 v[120:123], v233 offset:8192
	s_waitcnt lgkmcnt(3)
	v_mfma_f32_32x32x16_bf16 v[68:83], v[124:127], v[140:143], v[68:83]
	ds_read_b128 v[124:127], v234 offset:8192
	s_waitcnt lgkmcnt(3)
	v_mfma_f32_32x32x16_bf16 v[68:83], v[128:131], v[144:147], v[68:83]
	ds_read_b128 v[128:131], v235 offset:8192
	s_waitcnt lgkmcnt(3)
	v_mfma_f32_32x32x16_bf16 v[68:83], v[116:119], v[148:151], v[68:83]
	ds_read_b128 v[116:119], v190 offset:4096
	s_waitcnt lgkmcnt(3)
	v_mfma_f32_32x32x16_bf16 v[68:83], v[120:123], v[152:155], v[68:83]
	ds_read_b128 v[120:123], v229 offset:4096
	s_waitcnt lgkmcnt(3)
	v_mfma_f32_32x32x16_bf16 v[68:83], v[124:127], v[156:159], v[68:83]
	ds_read_b128 v[124:127], v230 offset:4096
	s_waitcnt lgkmcnt(3)
	v_mfma_f32_32x32x16_bf16 v[68:83], v[128:131], v[160:163], v[68:83]
	ds_read_b128 v[128:131], v231 offset:4096
	s_waitcnt lgkmcnt(3)
	v_mfma_f32_32x32x16_bf16 v[68:83], v[116:119], v[164:167], v[68:83]
	s_waitcnt lgkmcnt(2)
	v_mfma_f32_32x32x16_bf16 v[68:83], v[120:123], v[172:175], v[68:83]
	s_waitcnt lgkmcnt(1)
	v_mfma_f32_32x32x16_bf16 v[68:83], v[124:127], v[168:171], v[68:83]
	s_waitcnt lgkmcnt(0)
	v_mfma_f32_32x32x16_bf16 v[68:83], v[128:131], v[176:179], v[68:83]
	ds_read_b64_tr_b16 v[116:117], v191 offset:0
	ds_read_b64_tr_b16 v[118:119], v191 offset:2048
	ds_read_b64_tr_b16 v[120:121], v191 offset:4096
	ds_read_b64_tr_b16 v[122:123], v191 offset:6144
	ds_read_b64_tr_b16 v[124:125], v191 offset:8192
	ds_read_b64_tr_b16 v[126:127], v191 offset:10240
	ds_read_b64_tr_b16 v[128:129], v191 offset:12288
	ds_read_b64_tr_b16 v[130:131], v191 offset:14336
	s_setprio 0
	s_nop 7
	s_nop 3
	s_cmp_le_i32 s63, s28
	s_cbranch_scc1 .Lnomask_a0b0
	v_add_u32_e32 v251, s17, v220
	v_cmp_gt_i32_e32 vcc, 0, v251
	v_cmp_gt_i32_e64 s[98:99], 1, v251
	v_cmp_gt_i32_e64 s[100:101], 2, v251
	v_cndmask_b32_e32 v84, v84, v219, vcc
	v_cndmask_b32_e64 v85, v85, v219, s[98:99]
	v_cndmask_b32_e64 v86, v86, v219, s[100:101]
	v_cmp_gt_i32_e32 vcc, 3, v251
	v_cmp_gt_i32_e64 s[98:99], 8, v251
	v_cmp_gt_i32_e64 s[100:101], 9, v251
	v_cndmask_b32_e32 v87, v87, v219, vcc
	v_cndmask_b32_e64 v88, v88, v219, s[98:99]
	v_cndmask_b32_e64 v89, v89, v219, s[100:101]
	v_cmp_gt_i32_e32 vcc, 10, v251
	v_cmp_gt_i32_e64 s[98:99], 11, v251
	v_cmp_gt_i32_e64 s[100:101], 16, v251
	v_cndmask_b32_e32 v90, v90, v219, vcc
	v_cndmask_b32_e64 v91, v91, v219, s[98:99]
	v_cndmask_b32_e64 v92, v92, v219, s[100:101]
	v_cmp_gt_i32_e32 vcc, 17, v251
	v_cmp_gt_i32_e64 s[98:99], 18, v251
	v_cmp_gt_i32_e64 s[100:101], 19, v251
	v_cndmask_b32_e32 v93, v93, v219, vcc
	v_cndmask_b32_e64 v94, v94, v219, s[98:99]
	v_cndmask_b32_e64 v95, v95, v219, s[100:101]
	v_cmp_gt_i32_e32 vcc, 24, v251
	v_cmp_gt_i32_e64 s[98:99], 25, v251
	v_cmp_gt_i32_e64 s[100:101], 26, v251
	v_cndmask_b32_e32 v96, v96, v219, vcc
	v_cndmask_b32_e64 v97, v97, v219, s[98:99]
	v_cndmask_b32_e64 v98, v98, v219, s[100:101]
	v_cmp_gt_i32_e32 vcc, 27, v251
	v_cmp_gt_i32_e64 s[98:99], 32, v251
	v_cmp_gt_i32_e64 s[100:101], 33, v251
	v_cndmask_b32_e32 v99, v99, v219, vcc
	v_cndmask_b32_e64 v68, v68, v219, s[98:99]
	v_cndmask_b32_e64 v69, v69, v219, s[100:101]
	v_cmp_gt_i32_e32 vcc, 34, v251
	v_cmp_gt_i32_e64 s[98:99], 35, v251
	v_cmp_gt_i32_e64 s[100:101], 40, v251
	v_cndmask_b32_e32 v70, v70, v219, vcc
	v_cndmask_b32_e64 v71, v71, v219, s[98:99]
	v_cndmask_b32_e64 v72, v72, v219, s[100:101]
	v_cmp_gt_i32_e32 vcc, 41, v251
	v_cmp_gt_i32_e64 s[98:99], 42, v251
	v_cmp_gt_i32_e64 s[100:101], 43, v251
	v_cndmask_b32_e32 v73, v73, v219, vcc
	v_cndmask_b32_e64 v74, v74, v219, s[98:99]
	v_cndmask_b32_e64 v75, v75, v219, s[100:101]
	v_cmp_gt_i32_e32 vcc, 48, v251
	v_cmp_gt_i32_e64 s[98:99], 49, v251
	v_cmp_gt_i32_e64 s[100:101], 50, v251
	v_cndmask_b32_e32 v76, v76, v219, vcc
	v_cndmask_b32_e64 v77, v77, v219, s[98:99]
	v_cndmask_b32_e64 v78, v78, v219, s[100:101]
	v_cmp_gt_i32_e32 vcc, 51, v251
	v_cmp_gt_i32_e64 s[98:99], 56, v251
	v_cmp_gt_i32_e64 s[100:101], 57, v251
	v_cndmask_b32_e32 v79, v79, v219, vcc
	v_cndmask_b32_e64 v80, v80, v219, s[98:99]
	v_cndmask_b32_e64 v81, v81, v219, s[100:101]
	v_cmp_gt_i32_e32 vcc, 58, v251
	v_cmp_gt_i32_e64 s[98:99], 59, v251
	s_nop 1
	v_cndmask_b32_e32 v82, v82, v219, vcc
	v_cndmask_b32_e64 v83, v83, v219, s[98:99]
.Lnomask_a0b0:
	v_cmp_eq_f32_e32 vcc, 0, v223
	s_cmp_eq_u64 vcc, exec
	s_cbranch_scc0 .Lsub_a0b0
	v_exp_f32_e32 v100, v84
	v_exp_f32_e32 v101, v85
	v_exp_f32_e32 v102, v86
	v_exp_f32_e32 v103, v87
	v_exp_f32_e32 v104, v88
	v_exp_f32_e32 v105, v89
	v_exp_f32_e32 v106, v90
	v_exp_f32_e32 v107, v91
	v_exp_f32_e32 v108, v92
	v_exp_f32_e32 v109, v93
	v_exp_f32_e32 v110, v94
	v_exp_f32_e32 v111, v95
	v_exp_f32_e32 v112, v96
	v_exp_f32_e32 v113, v97
	v_exp_f32_e32 v114, v98
	v_exp_f32_e32 v115, v99
	v_add_f32_e32 v237, v100, v101
	v_add_f32_e32 v251, v102, v103
	v_add_f32_e32 v237, v237, v104
	v_add_f32_e32 v251, v251, v105
	v_add_f32_e32 v237, v237, v106
	v_add_f32_e32 v251, v251, v107
	v_add_f32_e32 v237, v237, v108
	v_add_f32_e32 v251, v251, v109
	v_add_f32_e32 v237, v237, v110
	v_add_f32_e32 v251, v251, v111
	v_add_f32_e32 v237, v237, v112
	v_add_f32_e32 v251, v251, v113
	v_add_f32_e32 v237, v237, v114
	v_add_f32_e32 v251, v251, v115
	v_add_f32_e32 v237, v237, v251
	v_cvt_pk_bf16_f32 v238, v100, v101
	v_cvt_pk_bf16_f32 v239, v102, v103
	v_cvt_pk_bf16_f32 v240, v104, v105
	v_cvt_pk_bf16_f32 v241, v106, v107
	v_cvt_pk_bf16_f32 v242, v108, v109
	v_cvt_pk_bf16_f32 v243, v110, v111
	v_cvt_pk_bf16_f32 v244, v112, v113
	v_cvt_pk_bf16_f32 v245, v114, v115
	s_nop 1
	v_permlane32_swap_b32_e32 v238, v240
	v_permlane32_swap_b32_e32 v239, v241
	v_permlane32_swap_b32_e32 v242, v244
	v_permlane32_swap_b32_e32 v243, v245
	v_exp_f32_e32 v100, v68
	v_exp_f32_e32 v101, v69
	v_exp_f32_e32 v102, v70
	v_exp_f32_e32 v103, v71
	v_exp_f32_e32 v104, v72
	v_exp_f32_e32 v105, v73
	v_exp_f32_e32 v106, v74
	v_exp_f32_e32 v107, v75
	v_exp_f32_e32 v108, v76
	v_exp_f32_e32 v109, v77
	v_exp_f32_e32 v110, v78
	v_exp_f32_e32 v111, v79
	v_exp_f32_e32 v112, v80
	v_exp_f32_e32 v113, v81
	v_exp_f32_e32 v114, v82
	v_exp_f32_e32 v115, v83
	v_add_f32_e32 v250, v100, v101
	v_add_f32_e32 v251, v102, v103
	v_add_f32_e32 v250, v250, v104
	v_add_f32_e32 v251, v251, v105
	v_add_f32_e32 v250, v250, v106
	v_add_f32_e32 v251, v251, v107
	v_add_f32_e32 v250, v250, v108
	v_add_f32_e32 v251, v251, v109
	v_add_f32_e32 v250, v250, v110
	v_add_f32_e32 v251, v251, v111
	v_add_f32_e32 v250, v250, v112
	v_add_f32_e32 v251, v251, v113
	v_add_f32_e32 v250, v250, v114
	v_add_f32_e32 v251, v251, v115
	v_add_f32_e32 v250, v250, v251
	v_cvt_pk_bf16_f32 v100, v100, v101
	v_cvt_pk_bf16_f32 v101, v102, v103
	v_cvt_pk_bf16_f32 v102, v104, v105
	v_cvt_pk_bf16_f32 v103, v106, v107
	v_cvt_pk_bf16_f32 v104, v108, v109
	v_cvt_pk_bf16_f32 v105, v110, v111
	v_cvt_pk_bf16_f32 v106, v112, v113
	v_cvt_pk_bf16_f32 v107, v114, v115
	s_nop 1
	v_permlane32_swap_b32_e32 v100, v102
	v_permlane32_swap_b32_e32 v101, v103
	v_permlane32_swap_b32_e32 v104, v106
	v_permlane32_swap_b32_e32 v105, v107
	s_branch .Lsum_a0b0

.Lsum_a0b0:
	v_add_f32_e32 v237, v237, v250
	v_cmp_gt_f32_e32 vcc, 0x5f800000, v237
	s_cmp_eq_u64 vcc, exec
	s_cbranch_scc0 .Lfb_a0b0
	s_cmp_lg_u32 s17, 0
	s_cbranch_scc1 .Lnotfirst_a0b0
	v_cmp_lt_f32_e32 vcc, 0x21800000, v237
	s_cmp_eq_u64 vcc, exec
	s_cbranch_scc0 .Lfb_a0b0
.Lnotfirst_a0b0:
	v_mov_b32_e32 v250, v237
	s_nop 1
	v_permlane32_swap_b32_e32 v237, v250
	v_add_f32_e32 v237, v237, v250
	v_add_f32_e32 v221, v237, v221
	v_mov_b32_e32 v222, v223
	s_setprio 3
	s_waitcnt lgkmcnt(6)
	v_mfma_f32_32x32x16_bf16 v[52:67], v[116:119], v[238:241], v[52:67]
	ds_read_b64_tr_b16 v[116:117], v191 offset:512
	ds_read_b64_tr_b16 v[118:119], v191 offset:2560
	s_waitcnt lgkmcnt(6)
	v_mfma_f32_32x32x16_bf16 v[52:67], v[120:123], v[242:245], v[52:67]
	ds_read_b64_tr_b16 v[120:121], v191 offset:4608
	ds_read_b64_tr_b16 v[122:123], v191 offset:6656
	s_waitcnt lgkmcnt(6)
	v_mfma_f32_32x32x16_bf16 v[52:67], v[124:127], v[100:103], v[52:67]
	ds_read_b64_tr_b16 v[124:125], v191 offset:8704
	ds_read_b64_tr_b16 v[126:127], v191 offset:10752
	s_waitcnt lgkmcnt(6)
	v_mfma_f32_32x32x16_bf16 v[52:67], v[128:131], v[104:107], v[52:67]
	ds_read_b64_tr_b16 v[128:129], v191 offset:12800
	ds_read_b64_tr_b16 v[130:131], v191 offset:14848
	s_waitcnt lgkmcnt(6)
	v_mfma_f32_32x32x16_bf16 v[36:51], v[116:119], v[238:241], v[36:51]
	ds_read_b64_tr_b16 v[116:117], v191 offset:1024
	ds_read_b64_tr_b16 v[118:119], v191 offset:3072
	s_waitcnt lgkmcnt(6)
	v_mfma_f32_32x32x16_bf16 v[36:51], v[120:123], v[242:245], v[36:51]
	ds_read_b64_tr_b16 v[120:121], v191 offset:5120
	ds_read_b64_tr_b16 v[122:123], v191 offset:7168
	s_waitcnt lgkmcnt(6)
	v_mfma_f32_32x32x16_bf16 v[36:51], v[124:127], v[100:103], v[36:51]
	ds_read_b64_tr_b16 v[124:125], v191 offset:9216
	ds_read_b64_tr_b16 v[126:127], v191 offset:11264
	s_waitcnt lgkmcnt(6)
	v_mfma_f32_32x32x16_bf16 v[36:51], v[128:131], v[104:107], v[36:51]
	ds_read_b64_tr_b16 v[128:129], v191 offset:13312
	ds_read_b64_tr_b16 v[130:131], v191 offset:15360
	s_waitcnt lgkmcnt(6)
	v_mfma_f32_32x32x16_bf16 v[20:35], v[116:119], v[238:241], v[20:35]
	ds_read_b64_tr_b16 v[116:117], v191 offset:1536
	ds_read_b64_tr_b16 v[118:119], v191 offset:3584
	s_waitcnt lgkmcnt(6)
	v_mfma_f32_32x32x16_bf16 v[20:35], v[120:123], v[242:245], v[20:35]
	ds_read_b64_tr_b16 v[120:121], v191 offset:5632
	ds_read_b64_tr_b16 v[122:123], v191 offset:7680
	s_waitcnt lgkmcnt(6)
	v_mfma_f32_32x32x16_bf16 v[20:35], v[124:127], v[100:103], v[20:35]
	ds_read_b64_tr_b16 v[124:125], v191 offset:9728
	ds_read_b64_tr_b16 v[126:127], v191 offset:11776
	s_waitcnt lgkmcnt(6)
	v_mfma_f32_32x32x16_bf16 v[20:35], v[128:131], v[104:107], v[20:35]
	ds_read_b64_tr_b16 v[128:129], v191 offset:13824
	ds_read_b64_tr_b16 v[130:131], v191 offset:15872
	s_waitcnt lgkmcnt(6)
	v_mfma_f32_32x32x16_bf16 v[4:19], v[116:119], v[238:241], v[4:19]
	s_waitcnt lgkmcnt(4)
	v_mfma_f32_32x32x16_bf16 v[4:19], v[120:123], v[242:245], v[4:19]
	s_waitcnt lgkmcnt(2)
	v_mfma_f32_32x32x16_bf16 v[4:19], v[124:127], v[100:103], v[4:19]
	s_waitcnt lgkmcnt(0)
	v_mfma_f32_32x32x16_bf16 v[4:19], v[128:131], v[104:107], v[4:19]
	s_setprio 0
	s_branch .Ltail2_a0b0

.LBB0_571:
	s_setprio 3
	ds_read_b128 v[116:119], v189 offset:24576
	ds_read_b128 v[120:123], v226 offset:24576
	ds_read_b128 v[124:127], v227 offset:24576
	ds_read_b128 v[128:131], v228 offset:24576
	s_waitcnt lgkmcnt(3)
	v_mfma_f32_32x32x16_bf16 v[84:99], v[116:119], v[132:135], 0
	ds_read_b128 v[116:119], v232 offset:24576
	s_waitcnt lgkmcnt(3)
	v_mfma_f32_32x32x16_bf16 v[84:99], v[120:123], v[136:139], v[84:99]
	ds_read_b128 v[120:123], v233 offset:24576
	s_waitcnt lgkmcnt(3)
	v_mfma_f32_32x32x16_bf16 v[84:99], v[124:127], v[140:143], v[84:99]
	ds_read_b128 v[124:127], v234 offset:24576
	s_waitcnt lgkmcnt(3)
	v_mfma_f32_32x32x16_bf16 v[84:99], v[128:131], v[144:147], v[84:99]
	ds_read_b128 v[128:131], v235 offset:24576
	s_waitcnt lgkmcnt(3)
	v_mfma_f32_32x32x16_bf16 v[84:99], v[116:119], v[148:151], v[84:99]
	ds_read_b128 v[116:119], v190 offset:24576
	s_waitcnt lgkmcnt(3)
	v_mfma_f32_32x32x16_bf16 v[84:99], v[120:123], v[152:155], v[84:99]
	ds_read_b128 v[120:123], v229 offset:24576
	s_waitcnt lgkmcnt(3)
	v_mfma_f32_32x32x16_bf16 v[84:99], v[124:127], v[156:159], v[84:99]
	ds_read_b128 v[124:127], v230 offset:24576
	s_waitcnt lgkmcnt(3)
	v_mfma_f32_32x32x16_bf16 v[84:99], v[128:131], v[160:163], v[84:99]
	ds_read_b128 v[128:131], v231 offset:24576
	s_waitcnt lgkmcnt(3)
	v_mfma_f32_32x32x16_bf16 v[84:99], v[116:119], v[164:167], v[84:99]
	ds_read_b128 v[116:119], v189 offset:32768
	s_waitcnt lgkmcnt(3)
	v_mfma_f32_32x32x16_bf16 v[84:99], v[120:123], v[172:175], v[84:99]
	ds_read_b128 v[120:123], v226 offset:32768
	s_waitcnt lgkmcnt(3)
	v_mfma_f32_32x32x16_bf16 v[84:99], v[124:127], v[168:171], v[84:99]
	ds_read_b128 v[124:127], v227 offset:32768
	s_waitcnt lgkmcnt(3)
	v_mfma_f32_32x32x16_bf16 v[84:99], v[128:131], v[176:179], v[84:99]
	ds_read_b128 v[128:131], v228 offset:32768
	s_waitcnt lgkmcnt(3)
	v_mfma_f32_32x32x16_bf16 v[68:83], v[116:119], v[132:135], 0
	ds_read_b128 v[116:119], v232 offset:32768
	s_waitcnt lgkmcnt(3)
	v_mfma_f32_32x32x16_bf16 v[68:83], v[120:123], v[136:139], v[68:83]
	ds_read_b128 v[120:123], v233 offset:32768
	s_waitcnt lgkmcnt(3)
	v_mfma_f32_32x32x16_bf16 v[68:83], v[124:127], v[140:143], v[68:83]
	ds_read_b128 v[124:127], v234 offset:32768
	s_waitcnt lgkmcnt(3)
	v_mfma_f32_32x32x16_bf16 v[68:83], v[128:131], v[144:147], v[68:83]
	ds_read_b128 v[128:131], v235 offset:32768
	s_waitcnt lgkmcnt(3)
	v_mfma_f32_32x32x16_bf16 v[68:83], v[116:119], v[148:151], v[68:83]
	ds_read_b128 v[116:119], v190 offset:28672
	s_waitcnt lgkmcnt(3)
	v_mfma_f32_32x32x16_bf16 v[68:83], v[120:123], v[152:155], v[68:83]
	ds_read_b128 v[120:123], v229 offset:28672
	s_waitcnt lgkmcnt(3)
	v_mfma_f32_32x32x16_bf16 v[68:83], v[124:127], v[156:159], v[68:83]
	ds_read_b128 v[124:127], v230 offset:28672
	s_waitcnt lgkmcnt(3)
	v_mfma_f32_32x32x16_bf16 v[68:83], v[128:131], v[160:163], v[68:83]
	ds_read_b128 v[128:131], v231 offset:28672
	s_waitcnt lgkmcnt(3)
	v_mfma_f32_32x32x16_bf16 v[68:83], v[116:119], v[164:167], v[68:83]
	s_waitcnt lgkmcnt(2)
	v_mfma_f32_32x32x16_bf16 v[68:83], v[120:123], v[172:175], v[68:83]
	s_waitcnt lgkmcnt(1)
	v_mfma_f32_32x32x16_bf16 v[68:83], v[124:127], v[168:171], v[68:83]
	s_waitcnt lgkmcnt(0)
	v_mfma_f32_32x32x16_bf16 v[68:83], v[128:131], v[176:179], v[68:83]
	ds_read_b64_tr_b16 v[116:117], v191 offset:16384
	ds_read_b64_tr_b16 v[118:119], v191 offset:18432
	ds_read_b64_tr_b16 v[120:121], v191 offset:20480
	ds_read_b64_tr_b16 v[122:123], v191 offset:22528
	ds_read_b64_tr_b16 v[124:125], v191 offset:24576
	ds_read_b64_tr_b16 v[126:127], v191 offset:26624
	ds_read_b64_tr_b16 v[128:129], v191 offset:28672
	ds_read_b64_tr_b16 v[130:131], v191 offset:30720
	s_setprio 0
	s_nop 7
	s_nop 3
	s_add_i32 s98, s63, 64
	s_cmp_le_i32 s98, s28
	s_cbranch_scc1 .Lnomask_a0b1
	v_add_u32_e32 v251, s17, v220
	v_add_u32_e32 v251, -64, v251
	v_cmp_gt_i32_e32 vcc, 0, v251
	v_cmp_gt_i32_e64 s[98:99], 1, v251
	v_cmp_gt_i32_e64 s[100:101], 2, v251
	v_cndmask_b32_e32 v84, v84, v219, vcc
	v_cndmask_b32_e64 v85, v85, v219, s[98:99]
	v_cndmask_b32_e64 v86, v86, v219, s[100:101]
	v_cmp_gt_i32_e32 vcc, 3, v251
	v_cmp_gt_i32_e64 s[98:99], 8, v251
	v_cmp_gt_i32_e64 s[100:101], 9, v251
	v_cndmask_b32_e32 v87, v87, v219, vcc
	v_cndmask_b32_e64 v88, v88, v219, s[98:99]
	v_cndmask_b32_e64 v89, v89, v219, s[100:101]
	v_cmp_gt_i32_e32 vcc, 10, v251
	v_cmp_gt_i32_e64 s[98:99], 11, v251
	v_cmp_gt_i32_e64 s[100:101], 16, v251
	v_cndmask_b32_e32 v90, v90, v219, vcc
	v_cndmask_b32_e64 v91, v91, v219, s[98:99]
	v_cndmask_b32_e64 v92, v92, v219, s[100:101]
	v_cmp_gt_i32_e32 vcc, 17, v251
	v_cmp_gt_i32_e64 s[98:99], 18, v251
	v_cmp_gt_i32_e64 s[100:101], 19, v251
	v_cndmask_b32_e32 v93, v93, v219, vcc
	v_cndmask_b32_e64 v94, v94, v219, s[98:99]
	v_cndmask_b32_e64 v95, v95, v219, s[100:101]
	v_cmp_gt_i32_e32 vcc, 24, v251
	v_cmp_gt_i32_e64 s[98:99], 25, v251
	v_cmp_gt_i32_e64 s[100:101], 26, v251
	v_cndmask_b32_e32 v96, v96, v219, vcc
	v_cndmask_b32_e64 v97, v97, v219, s[98:99]
	v_cndmask_b32_e64 v98, v98, v219, s[100:101]
	v_cmp_gt_i32_e32 vcc, 27, v251
	v_cmp_gt_i32_e64 s[98:99], 32, v251
	v_cmp_gt_i32_e64 s[100:101], 33, v251
	v_cndmask_b32_e32 v99, v99, v219, vcc
	v_cndmask_b32_e64 v68, v68, v219, s[98:99]
	v_cndmask_b32_e64 v69, v69, v219, s[100:101]
	v_cmp_gt_i32_e32 vcc, 34, v251
	v_cmp_gt_i32_e64 s[98:99], 35, v251
	v_cmp_gt_i32_e64 s[100:101], 40, v251
	v_cndmask_b32_e32 v70, v70, v219, vcc
	v_cndmask_b32_e64 v71, v71, v219, s[98:99]
	v_cndmask_b32_e64 v72, v72, v219, s[100:101]
	v_cmp_gt_i32_e32 vcc, 41, v251
	v_cmp_gt_i32_e64 s[98:99], 42, v251
	v_cmp_gt_i32_e64 s[100:101], 43, v251
	v_cndmask_b32_e32 v73, v73, v219, vcc
	v_cndmask_b32_e64 v74, v74, v219, s[98:99]
	v_cndmask_b32_e64 v75, v75, v219, s[100:101]
	v_cmp_gt_i32_e32 vcc, 48, v251
	v_cmp_gt_i32_e64 s[98:99], 49, v251
	v_cmp_gt_i32_e64 s[100:101], 50, v251
	v_cndmask_b32_e32 v76, v76, v219, vcc
	v_cndmask_b32_e64 v77, v77, v219, s[98:99]
	v_cndmask_b32_e64 v78, v78, v219, s[100:101]
	v_cmp_gt_i32_e32 vcc, 51, v251
	v_cmp_gt_i32_e64 s[98:99], 56, v251
	v_cmp_gt_i32_e64 s[100:101], 57, v251
	v_cndmask_b32_e32 v79, v79, v219, vcc
	v_cndmask_b32_e64 v80, v80, v219, s[98:99]
	v_cndmask_b32_e64 v81, v81, v219, s[100:101]
	v_cmp_gt_i32_e32 vcc, 58, v251
	v_cmp_gt_i32_e64 s[98:99], 59, v251
	s_nop 1
	v_cndmask_b32_e32 v82, v82, v219, vcc
	v_cndmask_b32_e64 v83, v83, v219, s[98:99]
.Lnomask_a0b1:
	v_cmp_eq_f32_e32 vcc, 0, v222
	s_cmp_eq_u64 vcc, exec
	s_cbranch_scc0 .Lsub_a0b1
	v_exp_f32_e32 v100, v84
	v_exp_f32_e32 v101, v85
	v_exp_f32_e32 v102, v86
	v_exp_f32_e32 v103, v87
	v_exp_f32_e32 v104, v88
	v_exp_f32_e32 v105, v89
	v_exp_f32_e32 v106, v90
	v_exp_f32_e32 v107, v91
	v_exp_f32_e32 v108, v92
	v_exp_f32_e32 v109, v93
	v_exp_f32_e32 v110, v94
	v_exp_f32_e32 v111, v95
	v_exp_f32_e32 v112, v96
	v_exp_f32_e32 v113, v97
	v_exp_f32_e32 v114, v98
	v_exp_f32_e32 v115, v99
	v_add_f32_e32 v237, v100, v101
	v_add_f32_e32 v251, v102, v103
	v_add_f32_e32 v237, v237, v104
	v_add_f32_e32 v251, v251, v105
	v_add_f32_e32 v237, v237, v106
	v_add_f32_e32 v251, v251, v107
	v_add_f32_e32 v237, v237, v108
	v_add_f32_e32 v251, v251, v109
	v_add_f32_e32 v237, v237, v110
	v_add_f32_e32 v251, v251, v111
	v_add_f32_e32 v237, v237, v112
	v_add_f32_e32 v251, v251, v113
	v_add_f32_e32 v237, v237, v114
	v_add_f32_e32 v251, v251, v115
	v_add_f32_e32 v237, v237, v251
	v_cvt_pk_bf16_f32 v238, v100, v101
	v_cvt_pk_bf16_f32 v239, v102, v103
	v_cvt_pk_bf16_f32 v240, v104, v105
	v_cvt_pk_bf16_f32 v241, v106, v107
	v_cvt_pk_bf16_f32 v242, v108, v109
	v_cvt_pk_bf16_f32 v243, v110, v111
	v_cvt_pk_bf16_f32 v244, v112, v113
	v_cvt_pk_bf16_f32 v245, v114, v115
	s_nop 1
	v_permlane32_swap_b32_e32 v238, v240
	v_permlane32_swap_b32_e32 v239, v241
	v_permlane32_swap_b32_e32 v242, v244
	v_permlane32_swap_b32_e32 v243, v245
	v_exp_f32_e32 v100, v68
	v_exp_f32_e32 v101, v69
	v_exp_f32_e32 v102, v70
	v_exp_f32_e32 v103, v71
	v_exp_f32_e32 v104, v72
	v_exp_f32_e32 v105, v73
	v_exp_f32_e32 v106, v74
	v_exp_f32_e32 v107, v75
	v_exp_f32_e32 v108, v76
	v_exp_f32_e32 v109, v77
	v_exp_f32_e32 v110, v78
	v_exp_f32_e32 v111, v79
	v_exp_f32_e32 v112, v80
	v_exp_f32_e32 v113, v81
	v_exp_f32_e32 v114, v82
	v_exp_f32_e32 v115, v83
	v_add_f32_e32 v250, v100, v101
	v_add_f32_e32 v251, v102, v103
	v_add_f32_e32 v250, v250, v104
	v_add_f32_e32 v251, v251, v105
	v_add_f32_e32 v250, v250, v106
	v_add_f32_e32 v251, v251, v107
	v_add_f32_e32 v250, v250, v108
	v_add_f32_e32 v251, v251, v109
	v_add_f32_e32 v250, v250, v110
	v_add_f32_e32 v251, v251, v111
	v_add_f32_e32 v250, v250, v112
	v_add_f32_e32 v251, v251, v113
	v_add_f32_e32 v250, v250, v114
	v_add_f32_e32 v251, v251, v115
	v_add_f32_e32 v250, v250, v251
	v_cvt_pk_bf16_f32 v100, v100, v101
	v_cvt_pk_bf16_f32 v101, v102, v103
	v_cvt_pk_bf16_f32 v102, v104, v105
	v_cvt_pk_bf16_f32 v103, v106, v107
	v_cvt_pk_bf16_f32 v104, v108, v109
	v_cvt_pk_bf16_f32 v105, v110, v111
	v_cvt_pk_bf16_f32 v106, v112, v113
	v_cvt_pk_bf16_f32 v107, v114, v115
	s_nop 1
	v_permlane32_swap_b32_e32 v100, v102
	v_permlane32_swap_b32_e32 v101, v103
	v_permlane32_swap_b32_e32 v104, v106
	v_permlane32_swap_b32_e32 v105, v107
	s_branch .Lsum_a0b1

.LBB0_1452:
	s_setprio 3
	ds_read_b128 v[140:143], v176
	ds_read_b128 v[144:147], v176 offset:32
	ds_read_b128 v[148:151], v176 offset:64
	ds_read_b128 v[152:155], v176 offset:96
	ds_read_b128 v[208:211], v172 offset:32768
	ds_read_b128 v[212:215], v206 offset:32768
	ds_read_b128 v[216:219], v207 offset:32768
	ds_read_b128 v[220:223], v237 offset:32768
	ds_read_b128 v[224:227], v244 offset:32768
	ds_read_b128 v[228:231], v245 offset:32768
	ds_read_b128 v[232:235], v246 offset:32768
	ds_read_b128 v[238:241], v247 offset:32768
	ds_read_b128 v[156:159], v176 offset:128
	ds_read_b128 v[160:163], v176 offset:160
	ds_read_b128 v[164:167], v176 offset:192
	ds_read_b128 v[168:171], v176 offset:224
	s_waitcnt lgkmcnt(11)
	v_mfma_f32_32x32x16_bf16 v[84:99], v[208:211], v[100:103], v[140:155]
	ds_read_b128 v[208:211], v172 offset:40960
	s_waitcnt lgkmcnt(11)
	v_mfma_f32_32x32x16_bf16 v[84:99], v[212:215], v[104:107], v[84:99]
	ds_read_b128 v[212:215], v206 offset:40960
	s_waitcnt lgkmcnt(11)
	v_mfma_f32_32x32x16_bf16 v[84:99], v[216:219], v[108:111], v[84:99]
	ds_read_b128 v[216:219], v207 offset:40960
	s_waitcnt lgkmcnt(11)
	v_mfma_f32_32x32x16_bf16 v[84:99], v[220:223], v[112:115], v[84:99]
	ds_read_b128 v[220:223], v237 offset:40960
	s_waitcnt lgkmcnt(11)
	v_mfma_f32_32x32x16_bf16 v[84:99], v[224:227], v[116:119], v[84:99]
	ds_read_b128 v[224:227], v244 offset:40960
	s_waitcnt lgkmcnt(11)
	v_mfma_f32_32x32x16_bf16 v[84:99], v[228:231], v[120:123], v[84:99]
	ds_read_b128 v[228:231], v245 offset:40960
	s_waitcnt lgkmcnt(11)
	v_mfma_f32_32x32x16_bf16 v[84:99], v[232:235], v[124:127], v[84:99]
	ds_read_b128 v[232:235], v246 offset:40960
	s_waitcnt lgkmcnt(11)
	v_mfma_f32_32x32x16_bf16 v[84:99], v[238:241], v[128:131], v[84:99]
	ds_read_b128 v[238:241], v247 offset:40960
	s_waitcnt lgkmcnt(7)
	v_mfma_f32_32x32x16_bf16 v[68:83], v[208:211], v[100:103], v[156:171]
	s_waitcnt lgkmcnt(6)
	v_mfma_f32_32x32x16_bf16 v[68:83], v[212:215], v[104:107], v[68:83]
	s_waitcnt lgkmcnt(5)
	v_mfma_f32_32x32x16_bf16 v[68:83], v[216:219], v[108:111], v[68:83]
	s_waitcnt lgkmcnt(4)
	v_mfma_f32_32x32x16_bf16 v[68:83], v[220:223], v[112:115], v[68:83]
	s_waitcnt lgkmcnt(3)
	v_mfma_f32_32x32x16_bf16 v[68:83], v[224:227], v[116:119], v[68:83]
	s_waitcnt lgkmcnt(2)
	v_mfma_f32_32x32x16_bf16 v[68:83], v[228:231], v[120:123], v[68:83]
	s_waitcnt lgkmcnt(1)
	v_mfma_f32_32x32x16_bf16 v[68:83], v[232:235], v[124:127], v[68:83]
	s_waitcnt lgkmcnt(0)
	v_mfma_f32_32x32x16_bf16 v[68:83], v[238:241], v[128:131], v[68:83]
	ds_read_b64_tr_b16 v[208:209], v174 offset:0
	ds_read_b64_tr_b16 v[210:211], v174 offset:2048
	ds_read_b64_tr_b16 v[212:213], v174 offset:4096
	ds_read_b64_tr_b16 v[214:215], v174 offset:6144
	ds_read_b64_tr_b16 v[216:217], v174 offset:8192
	ds_read_b64_tr_b16 v[218:219], v174 offset:10240
	ds_read_b64_tr_b16 v[220:221], v174 offset:12288
	ds_read_b64_tr_b16 v[222:223], v174 offset:14336
	s_setprio 0
	s_nop 7
	s_nop 3
	s_cmp_le_i32 s18, s40
	s_cbranch_scc1 .Lnomask_a1b0
	v_add_u32_e32 v250, s71, v190
	v_cmp_gt_i32_e32 vcc, 0, v250
	v_cmp_gt_i32_e64 s[98:99], 1, v250
	v_cmp_gt_i32_e64 s[100:101], 2, v250
	v_cndmask_b32_e32 v84, v84, v189, vcc
	v_cndmask_b32_e64 v85, v85, v189, s[98:99]
	v_cndmask_b32_e64 v86, v86, v189, s[100:101]
	v_cmp_gt_i32_e32 vcc, 3, v250
	v_cmp_gt_i32_e64 s[98:99], 8, v250
	v_cmp_gt_i32_e64 s[100:101], 9, v250
	v_cndmask_b32_e32 v87, v87, v189, vcc
	v_cndmask_b32_e64 v88, v88, v189, s[98:99]
	v_cndmask_b32_e64 v89, v89, v189, s[100:101]
	v_cmp_gt_i32_e32 vcc, 10, v250
	v_cmp_gt_i32_e64 s[98:99], 11, v250
	v_cmp_gt_i32_e64 s[100:101], 16, v250
	v_cndmask_b32_e32 v90, v90, v189, vcc
	v_cndmask_b32_e64 v91, v91, v189, s[98:99]
	v_cndmask_b32_e64 v92, v92, v189, s[100:101]
	v_cmp_gt_i32_e32 vcc, 17, v250
	v_cmp_gt_i32_e64 s[98:99], 18, v250
	v_cmp_gt_i32_e64 s[100:101], 19, v250
	v_cndmask_b32_e32 v93, v93, v189, vcc
	v_cndmask_b32_e64 v94, v94, v189, s[98:99]
	v_cndmask_b32_e64 v95, v95, v189, s[100:101]
	v_cmp_gt_i32_e32 vcc, 24, v250
	v_cmp_gt_i32_e64 s[98:99], 25, v250
	v_cmp_gt_i32_e64 s[100:101], 26, v250
	v_cndmask_b32_e32 v96, v96, v189, vcc
	v_cndmask_b32_e64 v97, v97, v189, s[98:99]
	v_cndmask_b32_e64 v98, v98, v189, s[100:101]
	v_cmp_gt_i32_e32 vcc, 27, v250
	v_cmp_gt_i32_e64 s[98:99], 32, v250
	v_cmp_gt_i32_e64 s[100:101], 33, v250
	v_cndmask_b32_e32 v99, v99, v189, vcc
	v_cndmask_b32_e64 v68, v68, v189, s[98:99]
	v_cndmask_b32_e64 v69, v69, v189, s[100:101]
	v_cmp_gt_i32_e32 vcc, 34, v250
	v_cmp_gt_i32_e64 s[98:99], 35, v250
	v_cmp_gt_i32_e64 s[100:101], 40, v250
	v_cndmask_b32_e32 v70, v70, v189, vcc
	v_cndmask_b32_e64 v71, v71, v189, s[98:99]
	v_cndmask_b32_e64 v72, v72, v189, s[100:101]
	v_cmp_gt_i32_e32 vcc, 41, v250
	v_cmp_gt_i32_e64 s[98:99], 42, v250
	v_cmp_gt_i32_e64 s[100:101], 43, v250
	v_cndmask_b32_e32 v73, v73, v189, vcc
	v_cndmask_b32_e64 v74, v74, v189, s[98:99]
	v_cndmask_b32_e64 v75, v75, v189, s[100:101]
	v_cmp_gt_i32_e32 vcc, 48, v250
	v_cmp_gt_i32_e64 s[98:99], 49, v250
	v_cmp_gt_i32_e64 s[100:101], 50, v250
	v_cndmask_b32_e32 v76, v76, v189, vcc
	v_cndmask_b32_e64 v77, v77, v189, s[98:99]
	v_cndmask_b32_e64 v78, v78, v189, s[100:101]
	v_cmp_gt_i32_e32 vcc, 51, v250
	v_cmp_gt_i32_e64 s[98:99], 56, v250
	v_cmp_gt_i32_e64 s[100:101], 57, v250
	v_cndmask_b32_e32 v79, v79, v189, vcc
	v_cndmask_b32_e64 v80, v80, v189, s[98:99]
	v_cndmask_b32_e64 v81, v81, v189, s[100:101]
	v_cmp_gt_i32_e32 vcc, 58, v250
	v_cmp_gt_i32_e64 s[98:99], 59, v250
	s_nop 1
	v_cndmask_b32_e32 v82, v82, v189, vcc
	v_cndmask_b32_e64 v83, v83, v189, s[98:99]
.Lnomask_a1b0:
	v_cmp_eq_f32_e32 vcc, 0, v193
	s_cmp_eq_u64 vcc, exec
	s_cbranch_scc0 .Lsub_a1b0
	v_exp_f32_e32 v140, v84
	v_exp_f32_e32 v141, v85
	v_exp_f32_e32 v142, v86
	v_exp_f32_e32 v143, v87
	v_exp_f32_e32 v144, v88
	v_exp_f32_e32 v145, v89
	v_exp_f32_e32 v146, v90
	v_exp_f32_e32 v147, v91
	v_exp_f32_e32 v148, v92
	v_exp_f32_e32 v149, v93
	v_exp_f32_e32 v150, v94
	v_exp_f32_e32 v151, v95
	v_exp_f32_e32 v152, v96
	v_exp_f32_e32 v153, v97
	v_exp_f32_e32 v154, v98
	v_exp_f32_e32 v155, v99
	v_add_f32_e32 v248, v140, v141
	v_add_f32_e32 v250, v142, v143
	v_add_f32_e32 v248, v248, v144
	v_add_f32_e32 v250, v250, v145
	v_add_f32_e32 v248, v248, v146
	v_add_f32_e32 v250, v250, v147
	v_add_f32_e32 v248, v248, v148
	v_add_f32_e32 v250, v250, v149
	v_add_f32_e32 v248, v248, v150
	v_add_f32_e32 v250, v250, v151
	v_add_f32_e32 v248, v248, v152
	v_add_f32_e32 v250, v250, v153
	v_add_f32_e32 v248, v248, v154
	v_add_f32_e32 v250, v250, v155
	v_add_f32_e32 v248, v248, v250
	v_cvt_pk_bf16_f32 v140, v140, v141
	v_cvt_pk_bf16_f32 v141, v142, v143
	v_cvt_pk_bf16_f32 v142, v144, v145
	v_cvt_pk_bf16_f32 v143, v146, v147
	v_cvt_pk_bf16_f32 v144, v148, v149
	v_cvt_pk_bf16_f32 v145, v150, v151
	v_cvt_pk_bf16_f32 v146, v152, v153
	v_cvt_pk_bf16_f32 v147, v154, v155
	s_nop 1
	v_permlane32_swap_b32_e32 v140, v142
	v_permlane32_swap_b32_e32 v141, v143
	v_permlane32_swap_b32_e32 v144, v146
	v_permlane32_swap_b32_e32 v145, v147
	v_exp_f32_e32 v156, v68
	v_exp_f32_e32 v157, v69
	v_exp_f32_e32 v158, v70
	v_exp_f32_e32 v159, v71
	v_exp_f32_e32 v160, v72
	v_exp_f32_e32 v161, v73
	v_exp_f32_e32 v162, v74
	v_exp_f32_e32 v163, v75
	v_exp_f32_e32 v164, v76
	v_exp_f32_e32 v165, v77
	v_exp_f32_e32 v166, v78
	v_exp_f32_e32 v167, v79
	v_exp_f32_e32 v168, v80
	v_exp_f32_e32 v169, v81
	v_exp_f32_e32 v170, v82
	v_exp_f32_e32 v171, v83
	v_add_f32_e32 v249, v156, v157
	v_add_f32_e32 v250, v158, v159
	v_add_f32_e32 v249, v249, v160
	v_add_f32_e32 v250, v250, v161
	v_add_f32_e32 v249, v249, v162
	v_add_f32_e32 v250, v250, v163
	v_add_f32_e32 v249, v249, v164
	v_add_f32_e32 v250, v250, v165
	v_add_f32_e32 v249, v249, v166
	v_add_f32_e32 v250, v250, v167
	v_add_f32_e32 v249, v249, v168
	v_add_f32_e32 v250, v250, v169
	v_add_f32_e32 v249, v249, v170
	v_add_f32_e32 v250, v250, v171
	v_add_f32_e32 v249, v249, v250
	v_cvt_pk_bf16_f32 v156, v156, v157
	v_cvt_pk_bf16_f32 v157, v158, v159
	v_cvt_pk_bf16_f32 v158, v160, v161
	v_cvt_pk_bf16_f32 v159, v162, v163
	v_cvt_pk_bf16_f32 v160, v164, v165
	v_cvt_pk_bf16_f32 v161, v166, v167
	v_cvt_pk_bf16_f32 v162, v168, v169
	v_cvt_pk_bf16_f32 v163, v170, v171
	s_nop 1
	v_permlane32_swap_b32_e32 v156, v158
	v_permlane32_swap_b32_e32 v157, v159
	v_permlane32_swap_b32_e32 v160, v162
	v_permlane32_swap_b32_e32 v161, v163
	s_branch .Lsum_a1b0

.Lsum_a1b0:
	v_add_f32_e32 v248, v248, v249
	v_cmp_gt_f32_e32 vcc, 0x5f800000, v248
	s_cmp_eq_u64 vcc, exec
	s_cbranch_scc0 .Lfb_a1b0
	s_cmp_lg_u32 s71, 0
	s_cbranch_scc1 .Lnotfirst_a1b0
	v_cmp_lt_f32_e32 vcc, 0x21800000, v248
	s_cmp_eq_u64 vcc, exec
	s_cbranch_scc0 .Lfb_a1b0
.Lnotfirst_a1b0:
	v_mov_b32_e32 v249, v248
	s_nop 1
	v_permlane32_swap_b32_e32 v248, v249
	v_add_f32_e32 v248, v248, v249
	v_add_f32_e32 v191, v248, v191
	v_mov_b32_e32 v192, v193
	s_setprio 3
	s_waitcnt lgkmcnt(6)
	v_mfma_f32_32x32x16_bf16 v[52:67], v[208:211], v[140:143], v[52:67]
	ds_read_b64_tr_b16 v[208:209], v174 offset:512
	ds_read_b64_tr_b16 v[210:211], v174 offset:2560
	s_waitcnt lgkmcnt(6)
	v_mfma_f32_32x32x16_bf16 v[52:67], v[212:215], v[144:147], v[52:67]
	ds_read_b64_tr_b16 v[212:213], v174 offset:4608
	ds_read_b64_tr_b16 v[214:215], v174 offset:6656
	s_waitcnt lgkmcnt(6)
	v_mfma_f32_32x32x16_bf16 v[52:67], v[216:219], v[156:159], v[52:67]
	ds_read_b64_tr_b16 v[216:217], v174 offset:8704
	ds_read_b64_tr_b16 v[218:219], v174 offset:10752
	s_waitcnt lgkmcnt(6)
	v_mfma_f32_32x32x16_bf16 v[52:67], v[220:223], v[160:163], v[52:67]
	ds_read_b64_tr_b16 v[220:221], v174 offset:12800
	ds_read_b64_tr_b16 v[222:223], v174 offset:14848
	s_waitcnt lgkmcnt(6)
	v_mfma_f32_32x32x16_bf16 v[36:51], v[208:211], v[140:143], v[36:51]
	ds_read_b64_tr_b16 v[208:209], v174 offset:1024
	ds_read_b64_tr_b16 v[210:211], v174 offset:3072
	s_waitcnt lgkmcnt(6)
	v_mfma_f32_32x32x16_bf16 v[36:51], v[212:215], v[144:147], v[36:51]
	ds_read_b64_tr_b16 v[212:213], v174 offset:5120
	ds_read_b64_tr_b16 v[214:215], v174 offset:7168
	s_waitcnt lgkmcnt(6)
	v_mfma_f32_32x32x16_bf16 v[36:51], v[216:219], v[156:159], v[36:51]
	ds_read_b64_tr_b16 v[216:217], v174 offset:9216
	ds_read_b64_tr_b16 v[218:219], v174 offset:11264
	s_waitcnt lgkmcnt(6)
	v_mfma_f32_32x32x16_bf16 v[36:51], v[220:223], v[160:163], v[36:51]
	ds_read_b64_tr_b16 v[220:221], v174 offset:13312
	ds_read_b64_tr_b16 v[222:223], v174 offset:15360
	s_waitcnt lgkmcnt(6)
	v_mfma_f32_32x32x16_bf16 v[20:35], v[208:211], v[140:143], v[20:35]
	ds_read_b64_tr_b16 v[208:209], v174 offset:1536
	ds_read_b64_tr_b16 v[210:211], v174 offset:3584
	s_waitcnt lgkmcnt(6)
	v_mfma_f32_32x32x16_bf16 v[20:35], v[212:215], v[144:147], v[20:35]
	ds_read_b64_tr_b16 v[212:213], v174 offset:5632
	ds_read_b64_tr_b16 v[214:215], v174 offset:7680
	s_waitcnt lgkmcnt(6)
	v_mfma_f32_32x32x16_bf16 v[20:35], v[216:219], v[156:159], v[20:35]
	ds_read_b64_tr_b16 v[216:217], v174 offset:9728
	ds_read_b64_tr_b16 v[218:219], v174 offset:11776
	s_waitcnt lgkmcnt(6)
	v_mfma_f32_32x32x16_bf16 v[20:35], v[220:223], v[160:163], v[20:35]
	ds_read_b64_tr_b16 v[220:221], v174 offset:13824
	ds_read_b64_tr_b16 v[222:223], v174 offset:15872
	s_waitcnt lgkmcnt(6)
	v_mfma_f32_32x32x16_bf16 v[4:19], v[208:211], v[140:143], v[4:19]
	s_waitcnt lgkmcnt(4)
	v_mfma_f32_32x32x16_bf16 v[4:19], v[212:215], v[144:147], v[4:19]
	s_waitcnt lgkmcnt(2)
	v_mfma_f32_32x32x16_bf16 v[4:19], v[216:219], v[156:159], v[4:19]
	s_waitcnt lgkmcnt(0)
	v_mfma_f32_32x32x16_bf16 v[4:19], v[220:223], v[160:163], v[4:19]
	s_setprio 0
	s_branch .Ltail2_a1b0

.LBB0_1467:
	s_setprio 3
	ds_read_b128 v[140:143], v177
	ds_read_b128 v[144:147], v177 offset:32
	ds_read_b128 v[148:151], v177 offset:64
	ds_read_b128 v[152:155], v177 offset:96
	ds_read_b128 v[208:211], v172 offset:49152
	ds_read_b128 v[212:215], v206 offset:49152
	ds_read_b128 v[216:219], v207 offset:49152
	ds_read_b128 v[220:223], v237 offset:49152
	ds_read_b128 v[224:227], v244 offset:49152
	ds_read_b128 v[228:231], v245 offset:49152
	ds_read_b128 v[232:235], v246 offset:49152
	ds_read_b128 v[238:241], v247 offset:49152
	ds_read_b128 v[156:159], v177 offset:128
	ds_read_b128 v[160:163], v177 offset:160
	ds_read_b128 v[164:167], v177 offset:192
	ds_read_b128 v[168:171], v177 offset:224
	s_waitcnt lgkmcnt(11)
	v_mfma_f32_32x32x16_bf16 v[84:99], v[208:211], v[100:103], v[140:155]
	ds_read_b128 v[208:211], v172 offset:57344
	s_waitcnt lgkmcnt(11)
	v_mfma_f32_32x32x16_bf16 v[84:99], v[212:215], v[104:107], v[84:99]
	ds_read_b128 v[212:215], v206 offset:57344
	s_waitcnt lgkmcnt(11)
	v_mfma_f32_32x32x16_bf16 v[84:99], v[216:219], v[108:111], v[84:99]
	ds_read_b128 v[216:219], v207 offset:57344
	s_waitcnt lgkmcnt(11)
	v_mfma_f32_32x32x16_bf16 v[84:99], v[220:223], v[112:115], v[84:99]
	ds_read_b128 v[220:223], v237 offset:57344
	s_waitcnt lgkmcnt(11)
	v_mfma_f32_32x32x16_bf16 v[84:99], v[224:227], v[116:119], v[84:99]
	ds_read_b128 v[224:227], v244 offset:57344
	s_waitcnt lgkmcnt(11)
	v_mfma_f32_32x32x16_bf16 v[84:99], v[228:231], v[120:123], v[84:99]
	ds_read_b128 v[228:231], v245 offset:57344
	s_waitcnt lgkmcnt(11)
	v_mfma_f32_32x32x16_bf16 v[84:99], v[232:235], v[124:127], v[84:99]
	ds_read_b128 v[232:235], v246 offset:57344
	s_waitcnt lgkmcnt(11)
	v_mfma_f32_32x32x16_bf16 v[84:99], v[238:241], v[128:131], v[84:99]
	ds_read_b128 v[238:241], v247 offset:57344
	s_waitcnt lgkmcnt(7)
	v_mfma_f32_32x32x16_bf16 v[68:83], v[208:211], v[100:103], v[156:171]
	s_waitcnt lgkmcnt(6)
	v_mfma_f32_32x32x16_bf16 v[68:83], v[212:215], v[104:107], v[68:83]
	s_waitcnt lgkmcnt(5)
	v_mfma_f32_32x32x16_bf16 v[68:83], v[216:219], v[108:111], v[68:83]
	s_waitcnt lgkmcnt(4)
	v_mfma_f32_32x32x16_bf16 v[68:83], v[220:223], v[112:115], v[68:83]
	s_waitcnt lgkmcnt(3)
	v_mfma_f32_32x32x16_bf16 v[68:83], v[224:227], v[116:119], v[68:83]
	s_waitcnt lgkmcnt(2)
	v_mfma_f32_32x32x16_bf16 v[68:83], v[228:231], v[120:123], v[68:83]
	s_waitcnt lgkmcnt(1)
	v_mfma_f32_32x32x16_bf16 v[68:83], v[232:235], v[124:127], v[68:83]
	s_waitcnt lgkmcnt(0)
	v_mfma_f32_32x32x16_bf16 v[68:83], v[238:241], v[128:131], v[68:83]
	ds_read_b64_tr_b16 v[208:209], v174 offset:16384
	ds_read_b64_tr_b16 v[210:211], v174 offset:18432
	ds_read_b64_tr_b16 v[212:213], v174 offset:20480
	ds_read_b64_tr_b16 v[214:215], v174 offset:22528
	ds_read_b64_tr_b16 v[216:217], v174 offset:24576
	ds_read_b64_tr_b16 v[218:219], v174 offset:26624
	ds_read_b64_tr_b16 v[220:221], v174 offset:28672
	ds_read_b64_tr_b16 v[222:223], v174 offset:30720
	s_setprio 0
	s_nop 7
	s_nop 3
	s_add_i32 s98, s18, 64
	s_cmp_le_i32 s98, s40
	s_cbranch_scc1 .Lnomask_a1b1
	v_add_u32_e32 v250, s71, v190
	v_add_u32_e32 v250, -64, v250
	v_cmp_gt_i32_e32 vcc, 0, v250
	v_cmp_gt_i32_e64 s[98:99], 1, v250
	v_cmp_gt_i32_e64 s[100:101], 2, v250
	v_cndmask_b32_e32 v84, v84, v189, vcc
	v_cndmask_b32_e64 v85, v85, v189, s[98:99]
	v_cndmask_b32_e64 v86, v86, v189, s[100:101]
	v_cmp_gt_i32_e32 vcc, 3, v250
	v_cmp_gt_i32_e64 s[98:99], 8, v250
	v_cmp_gt_i32_e64 s[100:101], 9, v250
	v_cndmask_b32_e32 v87, v87, v189, vcc
	v_cndmask_b32_e64 v88, v88, v189, s[98:99]
	v_cndmask_b32_e64 v89, v89, v189, s[100:101]
	v_cmp_gt_i32_e32 vcc, 10, v250
	v_cmp_gt_i32_e64 s[98:99], 11, v250
	v_cmp_gt_i32_e64 s[100:101], 16, v250
	v_cndmask_b32_e32 v90, v90, v189, vcc
	v_cndmask_b32_e64 v91, v91, v189, s[98:99]
	v_cndmask_b32_e64 v92, v92, v189, s[100:101]
	v_cmp_gt_i32_e32 vcc, 17, v250
	v_cmp_gt_i32_e64 s[98:99], 18, v250
	v_cmp_gt_i32_e64 s[100:101], 19, v250
	v_cndmask_b32_e32 v93, v93, v189, vcc
	v_cndmask_b32_e64 v94, v94, v189, s[98:99]
	v_cndmask_b32_e64 v95, v95, v189, s[100:101]
	v_cmp_gt_i32_e32 vcc, 24, v250
	v_cmp_gt_i32_e64 s[98:99], 25, v250
	v_cmp_gt_i32_e64 s[100:101], 26, v250
	v_cndmask_b32_e32 v96, v96, v189, vcc
	v_cndmask_b32_e64 v97, v97, v189, s[98:99]
	v_cndmask_b32_e64 v98, v98, v189, s[100:101]
	v_cmp_gt_i32_e32 vcc, 27, v250
	v_cmp_gt_i32_e64 s[98:99], 32, v250
	v_cmp_gt_i32_e64 s[100:101], 33, v250
	v_cndmask_b32_e32 v99, v99, v189, vcc
	v_cndmask_b32_e64 v68, v68, v189, s[98:99]
	v_cndmask_b32_e64 v69, v69, v189, s[100:101]
	v_cmp_gt_i32_e32 vcc, 34, v250
	v_cmp_gt_i32_e64 s[98:99], 35, v250
	v_cmp_gt_i32_e64 s[100:101], 40, v250
	v_cndmask_b32_e32 v70, v70, v189, vcc
	v_cndmask_b32_e64 v71, v71, v189, s[98:99]
	v_cndmask_b32_e64 v72, v72, v189, s[100:101]
	v_cmp_gt_i32_e32 vcc, 41, v250
	v_cmp_gt_i32_e64 s[98:99], 42, v250
	v_cmp_gt_i32_e64 s[100:101], 43, v250
	v_cndmask_b32_e32 v73, v73, v189, vcc
	v_cndmask_b32_e64 v74, v74, v189, s[98:99]
	v_cndmask_b32_e64 v75, v75, v189, s[100:101]
	v_cmp_gt_i32_e32 vcc, 48, v250
	v_cmp_gt_i32_e64 s[98:99], 49, v250
	v_cmp_gt_i32_e64 s[100:101], 50, v250
	v_cndmask_b32_e32 v76, v76, v189, vcc
	v_cndmask_b32_e64 v77, v77, v189, s[98:99]
	v_cndmask_b32_e64 v78, v78, v189, s[100:101]
	v_cmp_gt_i32_e32 vcc, 51, v250
	v_cmp_gt_i32_e64 s[98:99], 56, v250
	v_cmp_gt_i32_e64 s[100:101], 57, v250
	v_cndmask_b32_e32 v79, v79, v189, vcc
	v_cndmask_b32_e64 v80, v80, v189, s[98:99]
	v_cndmask_b32_e64 v81, v81, v189, s[100:101]
	v_cmp_gt_i32_e32 vcc, 58, v250
	v_cmp_gt_i32_e64 s[98:99], 59, v250
	s_nop 1
	v_cndmask_b32_e32 v82, v82, v189, vcc
	v_cndmask_b32_e64 v83, v83, v189, s[98:99]
.Lnomask_a1b1:
	v_cmp_eq_f32_e32 vcc, 0, v192
	s_cmp_eq_u64 vcc, exec
	s_cbranch_scc0 .Lsub_a1b1
	v_exp_f32_e32 v140, v84
	v_exp_f32_e32 v141, v85
	v_exp_f32_e32 v142, v86
	v_exp_f32_e32 v143, v87
	v_exp_f32_e32 v144, v88
	v_exp_f32_e32 v145, v89
	v_exp_f32_e32 v146, v90
	v_exp_f32_e32 v147, v91
	v_exp_f32_e32 v148, v92
	v_exp_f32_e32 v149, v93
	v_exp_f32_e32 v150, v94
	v_exp_f32_e32 v151, v95
	v_exp_f32_e32 v152, v96
	v_exp_f32_e32 v153, v97
	v_exp_f32_e32 v154, v98
	v_exp_f32_e32 v155, v99
	v_add_f32_e32 v248, v140, v141
	v_add_f32_e32 v250, v142, v143
	v_add_f32_e32 v248, v248, v144
	v_add_f32_e32 v250, v250, v145
	v_add_f32_e32 v248, v248, v146
	v_add_f32_e32 v250, v250, v147
	v_add_f32_e32 v248, v248, v148
	v_add_f32_e32 v250, v250, v149
	v_add_f32_e32 v248, v248, v150
	v_add_f32_e32 v250, v250, v151
	v_add_f32_e32 v248, v248, v152
	v_add_f32_e32 v250, v250, v153
	v_add_f32_e32 v248, v248, v154
	v_add_f32_e32 v250, v250, v155
	v_add_f32_e32 v248, v248, v250
	v_cvt_pk_bf16_f32 v140, v140, v141
	v_cvt_pk_bf16_f32 v141, v142, v143
	v_cvt_pk_bf16_f32 v142, v144, v145
	v_cvt_pk_bf16_f32 v143, v146, v147
	v_cvt_pk_bf16_f32 v144, v148, v149
	v_cvt_pk_bf16_f32 v145, v150, v151
	v_cvt_pk_bf16_f32 v146, v152, v153
	v_cvt_pk_bf16_f32 v147, v154, v155
	s_nop 1
	v_permlane32_swap_b32_e32 v140, v142
	v_permlane32_swap_b32_e32 v141, v143
	v_permlane32_swap_b32_e32 v144, v146
	v_permlane32_swap_b32_e32 v145, v147
	v_exp_f32_e32 v156, v68
	v_exp_f32_e32 v157, v69
	v_exp_f32_e32 v158, v70
	v_exp_f32_e32 v159, v71
	v_exp_f32_e32 v160, v72
	v_exp_f32_e32 v161, v73
	v_exp_f32_e32 v162, v74
	v_exp_f32_e32 v163, v75
	v_exp_f32_e32 v164, v76
	v_exp_f32_e32 v165, v77
	v_exp_f32_e32 v166, v78
	v_exp_f32_e32 v167, v79
	v_exp_f32_e32 v168, v80
	v_exp_f32_e32 v169, v81
	v_exp_f32_e32 v170, v82
	v_exp_f32_e32 v171, v83
	v_add_f32_e32 v249, v156, v157
	v_add_f32_e32 v250, v158, v159
	v_add_f32_e32 v249, v249, v160
	v_add_f32_e32 v250, v250, v161
	v_add_f32_e32 v249, v249, v162
	v_add_f32_e32 v250, v250, v163
	v_add_f32_e32 v249, v249, v164
	v_add_f32_e32 v250, v250, v165
	v_add_f32_e32 v249, v249, v166
	v_add_f32_e32 v250, v250, v167
	v_add_f32_e32 v249, v249, v168
	v_add_f32_e32 v250, v250, v169
	v_add_f32_e32 v249, v249, v170
	v_add_f32_e32 v250, v250, v171
	v_add_f32_e32 v249, v249, v250
	v_cvt_pk_bf16_f32 v156, v156, v157
	v_cvt_pk_bf16_f32 v157, v158, v159
	v_cvt_pk_bf16_f32 v158, v160, v161
	v_cvt_pk_bf16_f32 v159, v162, v163
	v_cvt_pk_bf16_f32 v160, v164, v165
	v_cvt_pk_bf16_f32 v161, v166, v167
	v_cvt_pk_bf16_f32 v162, v168, v169
	v_cvt_pk_bf16_f32 v163, v170, v171
	s_nop 1
	v_permlane32_swap_b32_e32 v156, v158
	v_permlane32_swap_b32_e32 v157, v159
	v_permlane32_swap_b32_e32 v160, v162
	v_permlane32_swap_b32_e32 v161, v163
	s_branch .Lsum_a1b1
